# speedup vs baseline: 1.0068x; 1.0068x over previous
.Lk2f_b2:
	s_waitcnt lgkmcnt(0)
	s_barrier
	v_and_b32_e32 v1, 63, v0
	v_lshlrev_b32_e32 v6, 3, v1
	ds_read_b64 v[14:15], v6 offset:18688
	s_cmp_eq_u32 s4, 7
	s_cbranch_scc1 .Lk2f_w7
	v_lshrrev_b32_e32 v3, 2, v1
	s_mul_i32 s5, s4, 14
	v_add_u32_e32 v6, s5, v3
	v_cmp_gt_u32_e32 vcc, 14, v3
	v_mov_b32_e32 v7, 0x7f
	v_mov_b32_e32 v8, 0x62
	v_and_b32_e32 v9, 3, v1
	v_cndmask_b32_e32 v7, v7, v6, vcc
	v_cndmask_b32_e32 v8, v8, v6, vcc
	v_lshlrev_b32_e32 v7, 2, v7
	v_mul_u32_u24_e32 v2, 0x90, v8
	ds_read_b32 v3, v7 offset:18688
	ds_read_b128 v[4:7], v2 offset:19456
	v_lshlrev_b32_e32 v1, 4, v9
	s_mov_b32 s32, s8
	s_and_b32 s33, s9, 0xffff
	s_mov_b32 s34, 0xc35000
	s_mov_b32 s35, 0x20000
	v_and_b32_e32 v8, 15, v0
	v_add_u32_e32 v9, s5, v8
	s_mul_i32 s6, s3, 0x62
	v_add_u32_e32 v9, s6, v9
	v_cmp_gt_u32_e32 vcc, 14, v8
	s_mov_b32 s7, 0x186a0
	v_cmp_gt_u32_e64 s[38:39], s7, v9
	s_and_b64 vcc, vcc, s[38:39]
	s_mov_b64 s[40:41], vcc
	v_and_b32_e32 v8, 0x30, v0
	v_cndmask_b32_e32 v9, 0, v9, vcc
	v_lshl_or_b32 v8, v9, 7, v8
	buffer_load_dwordx4 v[56:59], v8, s[32:35], 0 offen
	buffer_load_dwordx4 v[60:63], v8, s[32:35], 0 offen offset:64
	v_mov_b32_e32 v40, 0
	v_mov_b32_e32 v41, 0
	v_mov_b32_e32 v42, 0
	v_mov_b32_e32 v43, 0
	v_mov_b32_e32 v44, 0
	v_mov_b32_e32 v45, 0
	v_mov_b32_e32 v46, 0
	v_mov_b32_e32 v47, 0
	v_mov_b32_e32 v48, 0
	v_mov_b32_e32 v49, 0
	v_mov_b32_e32 v50, 0
	v_mov_b32_e32 v51, 0
	v_mov_b32_e32 v52, 0
	v_mov_b32_e32 v53, 0
	v_mov_b32_e32 v54, 0
	v_mov_b32_e32 v55, 0
	s_mov_b32 s5, 0
	s_mov_b32 s43, 0x7fffff80
	s_mov_b64 s[52:53], 0
	s_mov_b64 s[54:55], 0
	s_mov_b64 s[56:57], 0
	s_mov_b64 s[58:59], 0
	s_waitcnt lgkmcnt(0)
	v_max_u32_e32 v8, v14, v15
	v_cmp_lt_u32_e32 vcc, 32, v8
	s_cmp_lg_u64 vcc, 0
	s_cbranch_scc1 .Lk2f_fallback
	v_cmp_lt_i32_e32 vcc, 0, v3
	v_mov_b32_e32 v8, 0
	v_mov_b32_e32 v9, 0
	v_mov_b32_e32 v10, 0
	v_mov_b32_e32 v11, 0
	v_mov_b32_e32 v12, 0
	v_mov_b32_e32 v13, 0
	v_mov_b32_e32 v14, 0
	v_mov_b32_e32 v15, 0
	v_mov_b32_e32 v16, 0
	v_mov_b32_e32 v17, 0
	v_mov_b32_e32 v18, 0
	v_mov_b32_e32 v19, 0
	v_mov_b32_e32 v20, 0
	v_mov_b32_e32 v21, 0
	v_mov_b32_e32 v22, 0
	v_mov_b32_e32 v23, 0
	v_mov_b32_e32 v24, 0
	v_mov_b32_e32 v25, 0
	v_mov_b32_e32 v26, 0
	v_mov_b32_e32 v27, 0
	v_mov_b32_e32 v28, 0
	v_mov_b32_e32 v29, 0
	v_mov_b32_e32 v30, 0
	v_mov_b32_e32 v31, 0
	v_mov_b32_e32 v32, 0
	v_mov_b32_e32 v33, 0
	v_mov_b32_e32 v34, 0
	v_mov_b32_e32 v35, 0
	v_mov_b32_e32 v36, 0
	v_mov_b32_e32 v37, 0
	v_mov_b32_e32 v38, 0
	v_mov_b32_e32 v39, 0
	s_cmp_lg_u64 vcc, 0
	s_cbranch_scc0 .Lk2f_gdone
.Lk2f_loop:
	v_lshl_or_b32 v4, v4, 7, v1
	v_lshl_or_b32 v5, v5, 7, v1
	v_lshl_or_b32 v6, v6, 7, v1
	v_lshl_or_b32 v7, v7, 7, v1
	v_cmp_gt_u32_e64 s[44:45], s43, v4
	v_cmp_gt_u32_e64 s[46:47], s43, v5
	v_cmp_gt_u32_e64 s[48:49], s43, v6
	v_cmp_gt_u32_e64 s[50:51], s43, v7
	s_andn2_b64 s[60:61], s[52:53], s[44:45]
	s_andn2_b64 s[62:63], s[54:55], s[46:47]
	s_andn2_b64 s[64:65], s[56:57], s[48:49]
	s_andn2_b64 s[66:67], s[58:59], s[50:51]
	s_mov_b64 s[52:53], s[44:45]
	s_mov_b64 s[54:55], s[46:47]
	s_mov_b64 s[56:57], s[48:49]
	s_mov_b64 s[58:59], s[50:51]
	s_mov_b64 exec, s[60:61]
	s_cbranch_execz .Lx3_z0
	v_mov_b32_e32 v8, 0
	v_mov_b32_e32 v9, 0
	v_mov_b32_e32 v10, 0
	v_mov_b32_e32 v11, 0
	v_mov_b32_e32 v12, 0
	v_mov_b32_e32 v13, 0
	v_mov_b32_e32 v14, 0
	v_mov_b32_e32 v15, 0
.Lx3_z0:
	s_mov_b64 exec, s[62:63]
	s_cbranch_execz .Lx3_z1
	v_mov_b32_e32 v16, 0
	v_mov_b32_e32 v17, 0
	v_mov_b32_e32 v18, 0
	v_mov_b32_e32 v19, 0
	v_mov_b32_e32 v20, 0
	v_mov_b32_e32 v21, 0
	v_mov_b32_e32 v22, 0
	v_mov_b32_e32 v23, 0
.Lx3_z1:
	s_mov_b64 exec, s[64:65]
	s_cbranch_execz .Lx3_z2
	v_mov_b32_e32 v24, 0
	v_mov_b32_e32 v25, 0
	v_mov_b32_e32 v26, 0
	v_mov_b32_e32 v27, 0
	v_mov_b32_e32 v28, 0
	v_mov_b32_e32 v29, 0
	v_mov_b32_e32 v30, 0
	v_mov_b32_e32 v31, 0
.Lx3_z2:
	s_mov_b64 exec, s[66:67]
	s_cbranch_execz .Lx3_z3
	v_mov_b32_e32 v32, 0
	v_mov_b32_e32 v33, 0
	v_mov_b32_e32 v34, 0
	v_mov_b32_e32 v35, 0
	v_mov_b32_e32 v36, 0
	v_mov_b32_e32 v37, 0
	v_mov_b32_e32 v38, 0
	v_mov_b32_e32 v39, 0
.Lx3_z3:
	s_mov_b64 exec, s[44:45]
	s_cbranch_execz .Lx3_l0
	buffer_load_dwordx4 v[8:11], v4, s[32:35], 0 offen
	buffer_load_dwordx4 v[12:15], v4, s[32:35], 0 offen offset:64
.Lx3_l0:
	s_mov_b64 exec, s[46:47]
	s_cbranch_execz .Lx3_l1
	buffer_load_dwordx4 v[16:19], v5, s[32:35], 0 offen
	buffer_load_dwordx4 v[20:23], v5, s[32:35], 0 offen offset:64
.Lx3_l1:
	s_mov_b64 exec, s[48:49]
	s_cbranch_execz .Lx3_l2
	buffer_load_dwordx4 v[24:27], v6, s[32:35], 0 offen
	buffer_load_dwordx4 v[28:31], v6, s[32:35], 0 offen offset:64
.Lx3_l2:
	s_mov_b64 exec, s[50:51]
	s_cbranch_execz .Lx3_l3
	buffer_load_dwordx4 v[32:35], v7, s[32:35], 0 offen
	buffer_load_dwordx4 v[36:39], v7, s[32:35], 0 offen offset:64
.Lx3_l3:
	s_mov_b64 exec, -1
	v_add_u32_e32 v2, 16, v2
	s_add_i32 s5, s5, 4
	ds_read_b128 v[4:7], v2 offset:19456
	v_cmp_lt_i32_e32 vcc, s5, v3
	s_waitcnt vmcnt(0)
	v_pk_add_f16 v8, v8, v16
	v_pk_add_f16 v9, v9, v17
	v_pk_add_f16 v10, v10, v18
	v_pk_add_f16 v11, v11, v19
	s_waitcnt vmcnt(4)
	v_pk_add_f16 v12, v12, v20
	v_pk_add_f16 v13, v13, v21
	v_pk_add_f16 v14, v14, v22
	v_pk_add_f16 v15, v15, v23
	s_waitcnt vmcnt(1)
	v_pk_add_f16 v24, v24, v32
	v_pk_add_f16 v25, v25, v33
	v_pk_add_f16 v26, v26, v34
	v_pk_add_f16 v27, v27, v35
	v_pk_add_f16 v8, v8, v24
	v_pk_add_f16 v9, v9, v25
	v_pk_add_f16 v10, v10, v26
	v_pk_add_f16 v11, v11, v27
	s_waitcnt vmcnt(0)
	v_pk_add_f16 v28, v28, v36
	v_pk_add_f16 v29, v29, v37
	v_pk_add_f16 v30, v30, v38
	v_pk_add_f16 v31, v31, v39
	v_pk_add_f16 v12, v12, v28
	v_pk_add_f16 v13, v13, v29
	v_pk_add_f16 v14, v14, v30
	v_pk_add_f16 v15, v15, v31
	v_fma_mix_f32 v40, v8, 1.0, v40 op_sel:[0,0,0] op_sel_hi:[1,0,0]
	v_fma_mix_f32 v41, v8, 1.0, v41 op_sel:[1,0,0] op_sel_hi:[1,0,0]
	v_fma_mix_f32 v42, v9, 1.0, v42 op_sel:[0,0,0] op_sel_hi:[1,0,0]
	v_fma_mix_f32 v43, v9, 1.0, v43 op_sel:[1,0,0] op_sel_hi:[1,0,0]
	v_fma_mix_f32 v44, v10, 1.0, v44 op_sel:[0,0,0] op_sel_hi:[1,0,0]
	v_fma_mix_f32 v45, v10, 1.0, v45 op_sel:[1,0,0] op_sel_hi:[1,0,0]
	v_fma_mix_f32 v46, v11, 1.0, v46 op_sel:[0,0,0] op_sel_hi:[1,0,0]
	v_fma_mix_f32 v47, v11, 1.0, v47 op_sel:[1,0,0] op_sel_hi:[1,0,0]
	v_fma_mix_f32 v48, v12, 1.0, v48 op_sel:[0,0,0] op_sel_hi:[1,0,0]
	v_fma_mix_f32 v49, v12, 1.0, v49 op_sel:[1,0,0] op_sel_hi:[1,0,0]
	v_fma_mix_f32 v50, v13, 1.0, v50 op_sel:[0,0,0] op_sel_hi:[1,0,0]
	v_fma_mix_f32 v51, v13, 1.0, v51 op_sel:[1,0,0] op_sel_hi:[1,0,0]
	v_fma_mix_f32 v52, v14, 1.0, v52 op_sel:[0,0,0] op_sel_hi:[1,0,0]
	v_fma_mix_f32 v53, v14, 1.0, v53 op_sel:[1,0,0] op_sel_hi:[1,0,0]
	v_fma_mix_f32 v54, v15, 1.0, v54 op_sel:[0,0,0] op_sel_hi:[1,0,0]
	v_fma_mix_f32 v55, v15, 1.0, v55 op_sel:[1,0,0] op_sel_hi:[1,0,0]
	s_waitcnt lgkmcnt(0)
	s_cmp_lg_u64 vcc, 0
	s_cbranch_scc1 .Lk2f_loop
